# s22 + the back-to-back s_setprio 0 / s_setprio 1 pair in the middle of each 16-MFMA block removed (16 sites, four GEMM K-loops): no inserted issue slot between MFMAs
# speedup vs baseline: 1.0070x; 1.0049x over previous
; #define PG8_STAGE(bufoff, gbase, voff) do { _Pragma("unroll") for (int _i = 0; _i < 2; ++_i) \
;         __builtin_amdgcn_global_load_lds((const unsigned*)((const char*)(gbase) + (voff)[_i]), (LAS unsigned*)(lds + (bufoff) + ldsw + _i * 8192), 16, 0, 0); } while (0)
; #define PG8_LDA(dst, b, h) do { _Pragma("unroll") for (int m = 0; m < 4; ++m) _Pragma("unroll") for (int k = 0; k < 2; ++k) dst[m][k] = *(const LAS bf16x8*)(lds + PG8_SA(b, h) + aoff + m * 2048 + k * 1024); } while (0)
; #define PG8_LDB(dst, b, h) do { _Pragma("unroll") for (int n = 0; n < 2; ++n) _Pragma("unroll") for (int k = 0; k < 2; ++k) dst[n][k] = *(const LAS bf16x8*)(lds + PG8_SB(b, h) + boff + n * 2048 + k * 1024); } while (0)
; #define PG8_WAIT_V(n) asm volatile("s_waitcnt vmcnt(" #n ")" ::: "memory")
; #define PG8_WAIT_L(n) asm volatile("s_waitcnt lgkmcnt(" #n ")" ::: "memory")
; #define PG8_BAR __builtin_amdgcn_s_barrier()
; #define PG8_SCHED __builtin_amdgcn_sched_barrier(0)
;     ...
;             const bool last = (t == nt - 2);
;             const char* a1 = cA + (size_t)(t + 1) * kstep;
;             const char* a2 = last ? cA : cA + (size_t)(t + 2) * kstep; const char* b2 = last ? nB : cB + (size_t)(t + 2) * kstep;
;             const char* a3 = a2 + kstep; const char* b3 = b2 + kstep;
;             PG8_LDB(B0, 0, 0); PG8_LDB(B1, 0, 1); PG8_SCHED; PG8_LDA(At, 0, 0); PG8_STAGE(PG8_SA(1, 1), a1, va[1]);
;             if (last) {
; #pragma unroll
;                 for (int h = 0; h < 2; ++h)
; #pragma unroll
;                     for (int i = 0; i < 2; ++i) va[h][i] = vn[h][i]; }
;             PG8_WAIT_V(8); PG8_WAIT_L(0); PG8_BAR; PG8_MMA(0, 0, At, B0); PG8_MMA(0, 1, At, B1); PG8_BAR; PG8_SCHED;
;             PG8_LDA(At, 0, 1); PG8_STAGE(PG8_SB(0, 0), b2, voffB); PG8_STAGE(PG8_SB(0, 1), b2 + hstep, voffB); PG8_STAGE(PG8_SA(0, 0), a2, va[0]);
;             PG8_WAIT_V(8); PG8_WAIT_L(0); PG8_BAR; PG8_MMA(1, 0, At, B0); PG8_MMA(1, 1, At, B1); PG8_BAR; PG8_SCHED;
.LBB0_233:
	s_waitcnt vmcnt(8)
	s_add_u32 s44, s40, 0x80
	s_waitcnt lgkmcnt(0)
	s_addc_u32 s45, s41, 0
	s_and_b64 s[42:43], s[42:43], exec
	s_cselect_b32 s45, s1, s45
	s_cselect_b32 s44, s0, s44
	s_cselect_b32 s43, s9, s93
	s_cselect_b32 s42, s37, s92
	s_barrier
	s_setprio 1
	s_waitcnt lgkmcnt(0)
	v_mfma_f32_16x16x32_bf16 v[126:129], v[146:149], v[186:189], v[126:129]
	v_mfma_f32_16x16x32_bf16 v[122:125], v[154:157], v[186:189], v[122:125]
	v_mfma_f32_16x16x32_bf16 v[110:113], v[146:149], v[178:181], v[110:113]
	v_mfma_f32_16x16x32_bf16 v[106:109], v[154:157], v[178:181], v[106:109]
	v_mfma_f32_16x16x32_bf16 v[94:97], v[146:149], v[170:173], v[94:97]
	v_mfma_f32_16x16x32_bf16 v[90:93], v[154:157], v[170:173], v[90:93]
	v_mfma_f32_16x16x32_bf16 v[78:81], v[146:149], v[162:165], v[78:81]
	v_mfma_f32_16x16x32_bf16 v[74:77], v[154:157], v[162:165], v[74:77]
	v_mfma_f32_16x16x32_bf16 v[126:129], v[150:153], v[190:193], v[126:129]
	v_mfma_f32_16x16x32_bf16 v[122:125], v[158:161], v[190:193], v[122:125]
	v_mfma_f32_16x16x32_bf16 v[110:113], v[150:153], v[182:185], v[110:113]
	v_mfma_f32_16x16x32_bf16 v[106:109], v[158:161], v[182:185], v[106:109]
	v_mfma_f32_16x16x32_bf16 v[94:97], v[150:153], v[174:177], v[94:97]
	v_mfma_f32_16x16x32_bf16 v[90:93], v[158:161], v[174:177], v[90:93]
	v_mfma_f32_16x16x32_bf16 v[78:81], v[150:153], v[166:169], v[78:81]
	v_mfma_f32_16x16x32_bf16 v[74:77], v[158:161], v[166:169], v[74:77]
	v_mfma_f32_16x16x32_bf16 v[118:121], v[130:133], v[186:189], v[118:121]
	v_mfma_f32_16x16x32_bf16 v[114:117], v[138:141], v[186:189], v[114:117]
	v_mfma_f32_16x16x32_bf16 v[102:105], v[130:133], v[178:181], v[102:105]
	v_mfma_f32_16x16x32_bf16 v[98:101], v[138:141], v[178:181], v[98:101]
	v_mfma_f32_16x16x32_bf16 v[86:89], v[130:133], v[170:173], v[86:89]
	v_mfma_f32_16x16x32_bf16 v[82:85], v[138:141], v[170:173], v[82:85]
	v_mfma_f32_16x16x32_bf16 v[70:73], v[130:133], v[162:165], v[70:73]
	v_mfma_f32_16x16x32_bf16 v[66:69], v[138:141], v[162:165], v[66:69]
	v_mfma_f32_16x16x32_bf16 v[118:121], v[134:137], v[190:193], v[118:121]
	v_mfma_f32_16x16x32_bf16 v[114:117], v[142:145], v[190:193], v[114:117]
	v_mfma_f32_16x16x32_bf16 v[102:105], v[134:137], v[182:185], v[102:105]
	v_mfma_f32_16x16x32_bf16 v[98:101], v[142:145], v[182:185], v[98:101]
	v_mfma_f32_16x16x32_bf16 v[86:89], v[134:137], v[174:177], v[86:89]
	v_mfma_f32_16x16x32_bf16 v[82:85], v[142:145], v[174:177], v[82:85]
	v_mfma_f32_16x16x32_bf16 v[70:73], v[134:137], v[166:169], v[70:73]
	v_mfma_f32_16x16x32_bf16 v[66:69], v[142:145], v[166:169], v[66:69]
	s_setprio 0
	s_barrier
	s_mov_b32 m0, s25
	v_lshl_add_u64 v[228:229], s[42:43], 0, v[196:197]
	s_add_u32 vcc_lo, s42, 0x80000
	ds_read_b128 v[162:165], v224 offset:16384
	ds_read_b128 v[166:169], v224 offset:17408
	ds_read_b128 v[170:173], v224 offset:18432
	ds_read_b128 v[174:177], v224 offset:19456
	ds_read_b128 v[178:181], v224 offset:20480
	ds_read_b128 v[182:185], v224 offset:21504
	ds_read_b128 v[186:189], v224 offset:22528
	ds_read_b128 v[190:193], v224 offset:23552
	global_load_lds_dwordx4 v[228:229], off
	v_lshl_add_u64 v[230:231], s[42:43], 0, v[198:199]
	s_mov_b32 m0, s27
	s_addc_u32 vcc_hi, s43, 0
	global_load_lds_dwordx4 v[230:231], off
	v_lshl_add_u64 v[232:233], vcc, 0, v[196:197]
	s_mov_b32 m0, s29
	v_mov_b32_e32 v207, v201
	global_load_lds_dwordx4 v[232:233], off
	v_lshl_add_u64 v[232:233], vcc, 0, v[198:199]
	s_mov_b32 m0, s31
	v_lshl_add_u64 v[234:235], s[44:45], 0, v[206:207]
	global_load_lds_dwordx4 v[232:233], off
	s_mov_b32 m0, s23
	v_lshl_add_u64 v[232:233], s[44:45], 0, v[200:201]
	global_load_lds_dwordx4 v200, s[44:45]
	s_mov_b32 m0, s33
	s_nop 0
	global_load_lds_dwordx4 v206, s[44:45]
	s_waitcnt vmcnt(8)
	s_waitcnt lgkmcnt(0)
	s_barrier
	s_setprio 1
	s_waitcnt lgkmcnt(0)
	v_mfma_f32_16x16x32_bf16 v[62:65], v[146:149], v[162:165], v[62:65]
	v_mfma_f32_16x16x32_bf16 v[58:61], v[154:157], v[162:165], v[58:61]
	v_mfma_f32_16x16x32_bf16 v[46:49], v[146:149], v[170:173], v[46:49]
	v_mfma_f32_16x16x32_bf16 v[42:45], v[154:157], v[170:173], v[42:45]
	v_mfma_f32_16x16x32_bf16 v[30:33], v[146:149], v[178:181], v[30:33]
	v_mfma_f32_16x16x32_bf16 v[26:29], v[154:157], v[178:181], v[26:29]
	v_mfma_f32_16x16x32_bf16 v[14:17], v[146:149], v[186:189], v[14:17]
	v_mfma_f32_16x16x32_bf16 v[10:13], v[154:157], v[186:189], v[10:13]
	v_mfma_f32_16x16x32_bf16 v[62:65], v[150:153], v[166:169], v[62:65]
	v_mfma_f32_16x16x32_bf16 v[58:61], v[158:161], v[166:169], v[58:61]
	v_mfma_f32_16x16x32_bf16 v[46:49], v[150:153], v[174:177], v[46:49]
	v_mfma_f32_16x16x32_bf16 v[42:45], v[158:161], v[174:177], v[42:45]
	v_mfma_f32_16x16x32_bf16 v[30:33], v[150:153], v[182:185], v[30:33]
	v_mfma_f32_16x16x32_bf16 v[26:29], v[158:161], v[182:185], v[26:29]
	v_mfma_f32_16x16x32_bf16 v[14:17], v[150:153], v[190:193], v[14:17]
	v_mfma_f32_16x16x32_bf16 v[10:13], v[158:161], v[190:193], v[10:13]
	v_mfma_f32_16x16x32_bf16 v[54:57], v[130:133], v[162:165], v[54:57]
	v_mfma_f32_16x16x32_bf16 v[50:53], v[138:141], v[162:165], v[50:53]
	v_mfma_f32_16x16x32_bf16 v[38:41], v[130:133], v[170:173], v[38:41]
	v_mfma_f32_16x16x32_bf16 v[34:37], v[138:141], v[170:173], v[34:37]
	v_mfma_f32_16x16x32_bf16 v[22:25], v[130:133], v[178:181], v[22:25]
	v_mfma_f32_16x16x32_bf16 v[18:21], v[138:141], v[178:181], v[18:21]
	v_mfma_f32_16x16x32_bf16 v[6:9], v[130:133], v[186:189], v[6:9]
	v_mfma_f32_16x16x32_bf16 v[2:5], v[138:141], v[186:189], v[2:5]
	v_mfma_f32_16x16x32_bf16 v[54:57], v[134:137], v[166:169], v[54:57]
	v_mfma_f32_16x16x32_bf16 v[50:53], v[142:145], v[166:169], v[50:53]
	v_mfma_f32_16x16x32_bf16 v[38:41], v[134:137], v[174:177], v[38:41]
	v_mfma_f32_16x16x32_bf16 v[34:37], v[142:145], v[174:177], v[34:37]
	v_mfma_f32_16x16x32_bf16 v[22:25], v[134:137], v[182:185], v[22:25]
	v_mfma_f32_16x16x32_bf16 v[18:21], v[142:145], v[182:185], v[18:21]
	v_mfma_f32_16x16x32_bf16 v[6:9], v[134:137], v[190:193], v[6:9]
	v_mfma_f32_16x16x32_bf16 v[2:5], v[142:145], v[190:193], v[2:5]
	s_setprio 0
	s_barrier
; #define PG8_STAGE(bufoff, gbase, voff) do { _Pragma("unroll") for (int _i = 0; _i < 2; ++_i) \
;         __builtin_amdgcn_global_load_lds((const unsigned*)((const char*)(gbase) + (voff)[_i]), (LAS unsigned*)(lds + (bufoff) + ldsw + _i * 8192), 16, 0, 0); } while (0)
; #define PG8_LDA(dst, b, h) do { _Pragma("unroll") for (int m = 0; m < 4; ++m) _Pragma("unroll") for (int k = 0; k < 2; ++k) dst[m][k] = *(const LAS bf16x8*)(lds + PG8_SA(b, h) + aoff + m * 2048 + k * 1024); } while (0)
; #define PG8_LDB(dst, b, h) do { _Pragma("unroll") for (int n = 0; n < 2; ++n) _Pragma("unroll") for (int k = 0; k < 2; ++k) dst[n][k] = *(const LAS bf16x8*)(lds + PG8_SB(b, h) + boff + n * 2048 + k * 1024); } while (0)
; #define PG8_WAIT_V(n) asm volatile("s_waitcnt vmcnt(" #n ")" ::: "memory")
; #define PG8_WAIT_L(n) asm volatile("s_waitcnt lgkmcnt(" #n ")" ::: "memory")
; #define PG8_BAR __builtin_amdgcn_s_barrier()
; #define PG8_SCHED __builtin_amdgcn_sched_barrier(0)
;     ...
;             PG8_LDB(B0, 1, 0); PG8_LDB(B1, 1, 1); PG8_SCHED; PG8_LDA(At, 1, 0); PG8_STAGE(PG8_SA(0, 1), a2, va[1]);
;             PG8_WAIT_V(8); PG8_WAIT_L(0); PG8_BAR; PG8_MMA(0, 0, At, B0); PG8_MMA(0, 1, At, B1); PG8_BAR; PG8_SCHED;
	s_add_i32 s95, 0, 0x18000
	s_add_i32 vcc_lo, 0, 0x1c000
	v_add_u32_e32 v142, s95, v218
	v_add_u32_e32 v158, vcc_lo, v218
	ds_read_b128 v[130:133], v142
	ds_read_b128 v[134:137], v142 offset:1024
	ds_read_b128 v[138:141], v142 offset:2048
	ds_read_b128 v[142:145], v142 offset:3072
	ds_read_b128 v[146:149], v158
	ds_read_b128 v[150:153], v158 offset:1024
	ds_read_b128 v[154:157], v158 offset:2048
	ds_read_b128 v[158:161], v158 offset:3072
	s_mov_b32 m0, s35
	v_lshl_add_u64 v[214:215], s[44:45], 0, v[214:215]
	ds_read_b128 v[162:165], v224 offset:32768
	ds_read_b128 v[166:169], v224 offset:33792
	ds_read_b128 v[170:173], v224 offset:34816
	ds_read_b128 v[174:177], v224 offset:35840
	ds_read_b128 v[178:181], v224 offset:36864
	ds_read_b128 v[182:185], v224 offset:37888
	ds_read_b128 v[186:189], v224 offset:38912
	ds_read_b128 v[190:193], v224 offset:39936
	global_load_lds_dwordx4 v[214:215], off
	v_lshl_add_u64 v[212:213], s[44:45], 0, v[212:213]
	s_mov_b32 m0, s46
	s_nop 0
	global_load_lds_dwordx4 v[212:213], off
	s_waitcnt vmcnt(8)
	s_waitcnt lgkmcnt(0)
	s_barrier
	s_setprio 1
	s_waitcnt lgkmcnt(0)
	v_mfma_f32_16x16x32_bf16 v[126:129], v[130:133], v[162:165], v[126:129]
	v_mfma_f32_16x16x32_bf16 v[122:125], v[138:141], v[162:165], v[122:125]
	v_mfma_f32_16x16x32_bf16 v[110:113], v[130:133], v[170:173], v[110:113]
	v_mfma_f32_16x16x32_bf16 v[106:109], v[138:141], v[170:173], v[106:109]
	v_mfma_f32_16x16x32_bf16 v[94:97], v[130:133], v[178:181], v[94:97]
	v_mfma_f32_16x16x32_bf16 v[90:93], v[138:141], v[178:181], v[90:93]
	v_mfma_f32_16x16x32_bf16 v[78:81], v[130:133], v[186:189], v[78:81]
	v_mfma_f32_16x16x32_bf16 v[74:77], v[138:141], v[186:189], v[74:77]
	v_mfma_f32_16x16x32_bf16 v[126:129], v[134:137], v[166:169], v[126:129]
	v_mfma_f32_16x16x32_bf16 v[122:125], v[142:145], v[166:169], v[122:125]
	v_mfma_f32_16x16x32_bf16 v[110:113], v[134:137], v[174:177], v[110:113]
	v_mfma_f32_16x16x32_bf16 v[106:109], v[142:145], v[174:177], v[106:109]
	v_mfma_f32_16x16x32_bf16 v[94:97], v[134:137], v[182:185], v[94:97]
	v_mfma_f32_16x16x32_bf16 v[90:93], v[142:145], v[182:185], v[90:93]
	v_mfma_f32_16x16x32_bf16 v[78:81], v[134:137], v[190:193], v[78:81]
	v_mfma_f32_16x16x32_bf16 v[74:77], v[142:145], v[190:193], v[74:77]
	v_mfma_f32_16x16x32_bf16 v[118:121], v[146:149], v[162:165], v[118:121]
	v_mfma_f32_16x16x32_bf16 v[114:117], v[154:157], v[162:165], v[114:117]
	v_mfma_f32_16x16x32_bf16 v[102:105], v[146:149], v[170:173], v[102:105]
	v_mfma_f32_16x16x32_bf16 v[98:101], v[154:157], v[170:173], v[98:101]
	v_mfma_f32_16x16x32_bf16 v[86:89], v[146:149], v[178:181], v[86:89]
	v_mfma_f32_16x16x32_bf16 v[82:85], v[154:157], v[178:181], v[82:85]
	v_mfma_f32_16x16x32_bf16 v[70:73], v[146:149], v[186:189], v[70:73]
	v_mfma_f32_16x16x32_bf16 v[66:69], v[154:157], v[186:189], v[66:69]
	v_mfma_f32_16x16x32_bf16 v[118:121], v[150:153], v[166:169], v[118:121]
	v_mfma_f32_16x16x32_bf16 v[114:117], v[158:161], v[166:169], v[114:117]
	v_mfma_f32_16x16x32_bf16 v[102:105], v[150:153], v[174:177], v[102:105]
	v_mfma_f32_16x16x32_bf16 v[98:101], v[158:161], v[174:177], v[98:101]
	v_mfma_f32_16x16x32_bf16 v[86:89], v[150:153], v[182:185], v[86:89]
	v_mfma_f32_16x16x32_bf16 v[82:85], v[158:161], v[182:185], v[82:85]
	v_mfma_f32_16x16x32_bf16 v[70:73], v[150:153], v[190:193], v[70:73]
	v_mfma_f32_16x16x32_bf16 v[66:69], v[158:161], v[190:193], v[66:69]
	s_setprio 0
	s_barrier
; #define PG8_STAGE(bufoff, gbase, voff) do { _Pragma("unroll") for (int _i = 0; _i < 2; ++_i) \
;         __builtin_amdgcn_global_load_lds((const unsigned*)((const char*)(gbase) + (voff)[_i]), (LAS unsigned*)(lds + (bufoff) + ldsw + _i * 8192), 16, 0, 0); } while (0)
; #define PG8_LDA(dst, b, h) do { _Pragma("unroll") for (int m = 0; m < 4; ++m) _Pragma("unroll") for (int k = 0; k < 2; ++k) dst[m][k] = *(const LAS bf16x8*)(lds + PG8_SA(b, h) + aoff + m * 2048 + k * 1024); } while (0)
; #define PG8_WAIT_V(n) asm volatile("s_waitcnt vmcnt(" #n ")" ::: "memory")
; #define PG8_WAIT_L(n) asm volatile("s_waitcnt lgkmcnt(" #n ")" ::: "memory")
; #define PG8_BAR __builtin_amdgcn_s_barrier()
; #define PG8_SCHED __builtin_amdgcn_sched_barrier(0)
;     ...
;             PG8_LDA(At, 1, 1); PG8_STAGE(PG8_SB(1, 0), b3, voffB); PG8_STAGE(PG8_SB(1, 1), b3 + hstep, voffB); PG8_STAGE(PG8_SA(1, 0), a3, va[0]);
;             PG8_WAIT_V(8); PG8_WAIT_L(0); PG8_BAR; PG8_MMA(1, 0, At, B0); PG8_MMA(1, 1, At, B1); PG8_BAR; PG8_SCHED;
;         }
	s_add_i32 s44, s95, s2
	v_lshl_add_u64 v[212:213], v[228:229], 0, s[14:15]
	s_mov_b32 m0, s44
	ds_read_b128 v[162:165], v224 offset:49152
	ds_read_b128 v[166:169], v224 offset:50176
	ds_read_b128 v[170:173], v224 offset:51200
	ds_read_b128 v[174:177], v224 offset:52224
	ds_read_b128 v[178:181], v224 offset:53248
	ds_read_b128 v[182:185], v224 offset:54272
	ds_read_b128 v[186:189], v224 offset:55296
	ds_read_b128 v[190:193], v224 offset:56320
	global_load_lds_dwordx4 v[212:213], off
	s_add_i32 m0, s44, 0x2000
	s_add_u32 s42, s42, 0x80080
	v_lshl_add_u64 v[212:213], v[230:231], 0, s[14:15]
	s_addc_u32 s43, s43, 0
	s_add_i32 s44, vcc_lo, s2
	global_load_lds_dwordx4 v[212:213], off
	v_lshl_add_u64 v[212:213], s[42:43], 0, v[196:197]
	s_mov_b32 m0, s44
	s_nop 0
	global_load_lds_dwordx4 v[212:213], off
	v_lshl_add_u64 v[212:213], s[42:43], 0, v[198:199]
	s_add_i32 m0, s44, 0x2000
	s_nop 0
	global_load_lds_dwordx4 v[212:213], off
	v_lshl_add_u64 v[212:213], v[232:233], 0, s[14:15]
	s_mov_b32 m0, s51
	s_nop 0
	global_load_lds_dwordx4 v[212:213], off
	v_lshl_add_u64 v[212:213], v[234:235], 0, s[14:15]
	s_mov_b32 m0, s56
	s_nop 0
	global_load_lds_dwordx4 v[212:213], off
	s_waitcnt vmcnt(8)
	s_waitcnt lgkmcnt(0)
	s_barrier
	s_setprio 1
	s_waitcnt lgkmcnt(0)
	v_mfma_f32_16x16x32_bf16 v[62:65], v[130:133], v[162:165], v[62:65]
	v_mfma_f32_16x16x32_bf16 v[58:61], v[138:141], v[162:165], v[58:61]
	v_mfma_f32_16x16x32_bf16 v[46:49], v[130:133], v[170:173], v[46:49]
	v_mfma_f32_16x16x32_bf16 v[42:45], v[138:141], v[170:173], v[42:45]
	v_mfma_f32_16x16x32_bf16 v[30:33], v[130:133], v[178:181], v[30:33]
	v_mfma_f32_16x16x32_bf16 v[26:29], v[138:141], v[178:181], v[26:29]
	v_mfma_f32_16x16x32_bf16 v[14:17], v[130:133], v[186:189], v[14:17]
	v_mfma_f32_16x16x32_bf16 v[10:13], v[138:141], v[186:189], v[10:13]
	v_mfma_f32_16x16x32_bf16 v[62:65], v[134:137], v[166:169], v[62:65]
	v_mfma_f32_16x16x32_bf16 v[58:61], v[142:145], v[166:169], v[58:61]
	v_mfma_f32_16x16x32_bf16 v[46:49], v[134:137], v[174:177], v[46:49]
	v_mfma_f32_16x16x32_bf16 v[42:45], v[142:145], v[174:177], v[42:45]
	v_mfma_f32_16x16x32_bf16 v[30:33], v[134:137], v[182:185], v[30:33]
	v_mfma_f32_16x16x32_bf16 v[26:29], v[142:145], v[182:185], v[26:29]
	v_mfma_f32_16x16x32_bf16 v[14:17], v[134:137], v[190:193], v[14:17]
	v_mfma_f32_16x16x32_bf16 v[10:13], v[142:145], v[190:193], v[10:13]
	v_mfma_f32_16x16x32_bf16 v[54:57], v[146:149], v[162:165], v[54:57]
	v_mfma_f32_16x16x32_bf16 v[50:53], v[154:157], v[162:165], v[50:53]
	v_mfma_f32_16x16x32_bf16 v[38:41], v[146:149], v[170:173], v[38:41]
	v_mfma_f32_16x16x32_bf16 v[34:37], v[154:157], v[170:173], v[34:37]
	v_mfma_f32_16x16x32_bf16 v[22:25], v[146:149], v[178:181], v[22:25]
	v_mfma_f32_16x16x32_bf16 v[18:21], v[154:157], v[178:181], v[18:21]
	v_mfma_f32_16x16x32_bf16 v[6:9], v[146:149], v[186:189], v[6:9]
	v_mfma_f32_16x16x32_bf16 v[2:5], v[154:157], v[186:189], v[2:5]
	v_mfma_f32_16x16x32_bf16 v[54:57], v[150:153], v[166:169], v[54:57]
	v_mfma_f32_16x16x32_bf16 v[50:53], v[158:161], v[166:169], v[50:53]
	v_mfma_f32_16x16x32_bf16 v[38:41], v[150:153], v[174:177], v[38:41]
	v_mfma_f32_16x16x32_bf16 v[34:37], v[158:161], v[174:177], v[34:37]
	v_mfma_f32_16x16x32_bf16 v[22:25], v[150:153], v[182:185], v[22:25]
	v_mfma_f32_16x16x32_bf16 v[18:21], v[158:161], v[182:185], v[18:21]
	v_mfma_f32_16x16x32_bf16 v[6:9], v[150:153], v[190:193], v[6:9]
	v_mfma_f32_16x16x32_bf16 v[2:5], v[158:161], v[190:193], v[2:5]
	s_setprio 0
	s_barrier
	s_add_i32 s94, s94, 2
	s_add_u32 s92, s92, 0x100
	s_addc_u32 s93, s93, 0
	s_add_u32 s40, s40, 0x100
	s_addc_u32 s41, s41, 0
	s_cmp_gt_u32 s94, 29
	s_cbranch_scc1 .LBB0_236

; #define PG8_STAGE(bufoff, gbase, voff) do { _Pragma("unroll") for (int _i = 0; _i < 2; ++_i) \
;         __builtin_amdgcn_global_load_lds((const unsigned*)((const char*)(gbase) + (voff)[_i]), (LAS unsigned*)(lds + (bufoff) + ldsw + _i * 8192), 16, 0, 0); } while (0)
; #define PG8_LDA(dst, b, h) do { _Pragma("unroll") for (int m = 0; m < 4; ++m) _Pragma("unroll") for (int k = 0; k < 2; ++k) dst[m][k] = *(const LAS bf16x8*)(lds + PG8_SA(b, h) + aoff + m * 2048 + k * 1024); } while (0)
; #define PG8_LDB(dst, b, h) do { _Pragma("unroll") for (int n = 0; n < 2; ++n) _Pragma("unroll") for (int k = 0; k < 2; ++k) dst[n][k] = *(const LAS bf16x8*)(lds + PG8_SB(b, h) + boff + n * 2048 + k * 1024); } while (0)
; #define PG8_WAIT_V(n) asm volatile("s_waitcnt vmcnt(" #n ")" ::: "memory")
; #define PG8_WAIT_L(n) asm volatile("s_waitcnt lgkmcnt(" #n ")" ::: "memory")
; #define PG8_BAR __builtin_amdgcn_s_barrier()
; #define PG8_SCHED __builtin_amdgcn_sched_barrier(0)
;     ...
;             const bool last = (t == nt - 2);
;             const char* a1 = cA + (size_t)(t + 1) * kstep;
;             const char* a2 = last ? cA : cA + (size_t)(t + 2) * kstep; const char* b2 = last ? nB : cB + (size_t)(t + 2) * kstep;
;             const char* a3 = a2 + kstep; const char* b3 = b2 + kstep;
;             PG8_LDB(B0, 0, 0); PG8_LDB(B1, 0, 1); PG8_SCHED; PG8_LDA(At, 0, 0); PG8_STAGE(PG8_SA(1, 1), a1, va[1]);
;             if (last) {
; #pragma unroll
;                 for (int h = 0; h < 2; ++h)
; #pragma unroll
;                     for (int i = 0; i < 2; ++i) va[h][i] = vn[h][i]; }
;             PG8_WAIT_V(8); PG8_WAIT_L(0); PG8_BAR; PG8_MMA(0, 0, At, B0); PG8_MMA(0, 1, At, B1); PG8_BAR; PG8_SCHED;
;             PG8_LDA(At, 0, 1); PG8_STAGE(PG8_SB(0, 0), b2, voffB); PG8_STAGE(PG8_SB(0, 1), b2 + hstep, voffB); PG8_STAGE(PG8_SA(0, 0), a2, va[0]);
;             PG8_WAIT_V(8); PG8_WAIT_L(0); PG8_BAR; PG8_MMA(1, 0, At, B0); PG8_MMA(1, 1, At, B1); PG8_BAR; PG8_SCHED;
.LBB0_682:
	s_waitcnt vmcnt(8)
	s_add_u32 s36, s8, 0x80
	s_waitcnt lgkmcnt(0)
	s_addc_u32 s37, s9, 0
	s_and_b64 s[34:35], s[34:35], exec
	s_cselect_b32 s37, s1, s37
	s_cselect_b32 s36, s0, s36
	s_cselect_b32 s35, s29, s62
	s_cselect_b32 s34, s56, s57
	s_barrier
	s_setprio 1
	s_waitcnt lgkmcnt(0)
	v_mfma_f32_16x16x32_bf16 v[142:145], v[146:149], v[186:189], v[142:145]
	v_mfma_f32_16x16x32_bf16 v[138:141], v[154:157], v[186:189], v[138:141]
	v_mfma_f32_16x16x32_bf16 v[110:113], v[146:149], v[178:181], v[110:113]
	v_mfma_f32_16x16x32_bf16 v[106:109], v[154:157], v[178:181], v[106:109]
	v_mfma_f32_16x16x32_bf16 v[94:97], v[146:149], v[170:173], v[94:97]
	v_mfma_f32_16x16x32_bf16 v[90:93], v[154:157], v[170:173], v[90:93]
	v_mfma_f32_16x16x32_bf16 v[78:81], v[146:149], v[162:165], v[78:81]
	v_mfma_f32_16x16x32_bf16 v[74:77], v[154:157], v[162:165], v[74:77]
	v_mfma_f32_16x16x32_bf16 v[142:145], v[150:153], v[190:193], v[142:145]
	v_mfma_f32_16x16x32_bf16 v[138:141], v[158:161], v[190:193], v[138:141]
	v_mfma_f32_16x16x32_bf16 v[110:113], v[150:153], v[182:185], v[110:113]
	v_mfma_f32_16x16x32_bf16 v[106:109], v[158:161], v[182:185], v[106:109]
	v_mfma_f32_16x16x32_bf16 v[94:97], v[150:153], v[174:177], v[94:97]
	v_mfma_f32_16x16x32_bf16 v[90:93], v[158:161], v[174:177], v[90:93]
	v_mfma_f32_16x16x32_bf16 v[78:81], v[150:153], v[166:169], v[78:81]
	v_mfma_f32_16x16x32_bf16 v[74:77], v[158:161], v[166:169], v[74:77]
	v_mfma_f32_16x16x32_bf16 v[134:137], v[118:121], v[186:189], v[134:137]
	v_mfma_f32_16x16x32_bf16 v[114:117], v[126:129], v[186:189], v[114:117]
	v_mfma_f32_16x16x32_bf16 v[102:105], v[118:121], v[178:181], v[102:105]
	v_mfma_f32_16x16x32_bf16 v[98:101], v[126:129], v[178:181], v[98:101]
	v_mfma_f32_16x16x32_bf16 v[86:89], v[118:121], v[170:173], v[86:89]
	v_mfma_f32_16x16x32_bf16 v[82:85], v[126:129], v[170:173], v[82:85]
	v_mfma_f32_16x16x32_bf16 v[70:73], v[118:121], v[162:165], v[70:73]
	v_mfma_f32_16x16x32_bf16 v[66:69], v[126:129], v[162:165], v[66:69]
	v_mfma_f32_16x16x32_bf16 v[134:137], v[122:125], v[190:193], v[134:137]
	v_mfma_f32_16x16x32_bf16 v[114:117], v[130:133], v[190:193], v[114:117]
	v_mfma_f32_16x16x32_bf16 v[102:105], v[122:125], v[182:185], v[102:105]
	v_mfma_f32_16x16x32_bf16 v[98:101], v[130:133], v[182:185], v[98:101]
	v_mfma_f32_16x16x32_bf16 v[86:89], v[122:125], v[174:177], v[86:89]
	v_mfma_f32_16x16x32_bf16 v[82:85], v[130:133], v[174:177], v[82:85]
	v_mfma_f32_16x16x32_bf16 v[70:73], v[122:125], v[166:169], v[70:73]
	v_mfma_f32_16x16x32_bf16 v[66:69], v[130:133], v[166:169], v[66:69]
	s_setprio 0
	s_barrier
	s_mov_b32 m0, s39
	v_lshl_add_u64 v[232:233], s[34:35], 0, v[196:197]
	s_add_u32 s68, s34, 0x80000
	ds_read_b128 v[162:165], v228 offset:16384
	ds_read_b128 v[166:169], v228 offset:17408
	ds_read_b128 v[170:173], v228 offset:18432
	ds_read_b128 v[174:177], v228 offset:19456
	ds_read_b128 v[178:181], v228 offset:20480
	ds_read_b128 v[182:185], v228 offset:21504
	ds_read_b128 v[186:189], v228 offset:22528
	ds_read_b128 v[190:193], v228 offset:23552
	global_load_lds_dwordx4 v[232:233], off
	v_lshl_add_u64 v[234:235], s[34:35], 0, v[198:199]
	s_mov_b32 m0, s40
	s_addc_u32 s69, s35, 0
	global_load_lds_dwordx4 v[234:235], off
	v_lshl_add_u64 v[236:237], s[68:69], 0, v[196:197]
	s_mov_b32 m0, s41
	v_mov_b32_e32 v207, v201
	global_load_lds_dwordx4 v[236:237], off
	v_lshl_add_u64 v[236:237], s[68:69], 0, v[198:199]
	s_mov_b32 m0, s42
	v_lshl_add_u64 v[238:239], s[36:37], 0, v[206:207]
	global_load_lds_dwordx4 v[236:237], off
	s_mov_b32 m0, s38
	v_lshl_add_u64 v[236:237], s[36:37], 0, v[200:201]
	global_load_lds_dwordx4 v200, s[36:37]
	s_mov_b32 m0, s43
	s_nop 0
	global_load_lds_dwordx4 v206, s[36:37]
	s_waitcnt vmcnt(8)
	s_waitcnt lgkmcnt(0)
	s_barrier
	s_setprio 1
	s_waitcnt lgkmcnt(0)
	v_mfma_f32_16x16x32_bf16 v[62:65], v[146:149], v[162:165], v[62:65]
	v_mfma_f32_16x16x32_bf16 v[58:61], v[154:157], v[162:165], v[58:61]
	v_mfma_f32_16x16x32_bf16 v[46:49], v[146:149], v[170:173], v[46:49]
	v_mfma_f32_16x16x32_bf16 v[42:45], v[154:157], v[170:173], v[42:45]
	v_mfma_f32_16x16x32_bf16 v[30:33], v[146:149], v[178:181], v[30:33]
	v_mfma_f32_16x16x32_bf16 v[26:29], v[154:157], v[178:181], v[26:29]
	v_mfma_f32_16x16x32_bf16 v[14:17], v[146:149], v[186:189], v[14:17]
	v_mfma_f32_16x16x32_bf16 v[10:13], v[154:157], v[186:189], v[10:13]
	v_mfma_f32_16x16x32_bf16 v[62:65], v[150:153], v[166:169], v[62:65]
	v_mfma_f32_16x16x32_bf16 v[58:61], v[158:161], v[166:169], v[58:61]
	v_mfma_f32_16x16x32_bf16 v[46:49], v[150:153], v[174:177], v[46:49]
	v_mfma_f32_16x16x32_bf16 v[42:45], v[158:161], v[174:177], v[42:45]
	v_mfma_f32_16x16x32_bf16 v[30:33], v[150:153], v[182:185], v[30:33]
	v_mfma_f32_16x16x32_bf16 v[26:29], v[158:161], v[182:185], v[26:29]
	v_mfma_f32_16x16x32_bf16 v[14:17], v[150:153], v[190:193], v[14:17]
	v_mfma_f32_16x16x32_bf16 v[10:13], v[158:161], v[190:193], v[10:13]
	v_mfma_f32_16x16x32_bf16 v[54:57], v[118:121], v[162:165], v[54:57]
	v_mfma_f32_16x16x32_bf16 v[50:53], v[126:129], v[162:165], v[50:53]
	v_mfma_f32_16x16x32_bf16 v[38:41], v[118:121], v[170:173], v[38:41]
	v_mfma_f32_16x16x32_bf16 v[34:37], v[126:129], v[170:173], v[34:37]
	v_mfma_f32_16x16x32_bf16 v[22:25], v[118:121], v[178:181], v[22:25]
	v_mfma_f32_16x16x32_bf16 v[18:21], v[126:129], v[178:181], v[18:21]
	v_mfma_f32_16x16x32_bf16 v[6:9], v[118:121], v[186:189], v[6:9]
	v_mfma_f32_16x16x32_bf16 v[2:5], v[126:129], v[186:189], v[2:5]
	v_mfma_f32_16x16x32_bf16 v[54:57], v[122:125], v[166:169], v[54:57]
	v_mfma_f32_16x16x32_bf16 v[50:53], v[130:133], v[166:169], v[50:53]
	v_mfma_f32_16x16x32_bf16 v[38:41], v[122:125], v[174:177], v[38:41]
	v_mfma_f32_16x16x32_bf16 v[34:37], v[130:133], v[174:177], v[34:37]
	v_mfma_f32_16x16x32_bf16 v[22:25], v[122:125], v[182:185], v[22:25]
	v_mfma_f32_16x16x32_bf16 v[18:21], v[130:133], v[182:185], v[18:21]
	v_mfma_f32_16x16x32_bf16 v[6:9], v[122:125], v[190:193], v[6:9]
	v_mfma_f32_16x16x32_bf16 v[2:5], v[130:133], v[190:193], v[2:5]
	s_setprio 0
	s_barrier
; #define PG8_STAGE(bufoff, gbase, voff) do { _Pragma("unroll") for (int _i = 0; _i < 2; ++_i) \
;         __builtin_amdgcn_global_load_lds((const unsigned*)((const char*)(gbase) + (voff)[_i]), (LAS unsigned*)(lds + (bufoff) + ldsw + _i * 8192), 16, 0, 0); } while (0)
; #define PG8_LDA(dst, b, h) do { _Pragma("unroll") for (int m = 0; m < 4; ++m) _Pragma("unroll") for (int k = 0; k < 2; ++k) dst[m][k] = *(const LAS bf16x8*)(lds + PG8_SA(b, h) + aoff + m * 2048 + k * 1024); } while (0)
; #define PG8_LDB(dst, b, h) do { _Pragma("unroll") for (int n = 0; n < 2; ++n) _Pragma("unroll") for (int k = 0; k < 2; ++k) dst[n][k] = *(const LAS bf16x8*)(lds + PG8_SB(b, h) + boff + n * 2048 + k * 1024); } while (0)
; #define PG8_WAIT_V(n) asm volatile("s_waitcnt vmcnt(" #n ")" ::: "memory")
; #define PG8_WAIT_L(n) asm volatile("s_waitcnt lgkmcnt(" #n ")" ::: "memory")
; #define PG8_BAR __builtin_amdgcn_s_barrier()
; #define PG8_SCHED __builtin_amdgcn_sched_barrier(0)
;     ...
;             PG8_LDB(B0, 1, 0); PG8_LDB(B1, 1, 1); PG8_SCHED; PG8_LDA(At, 1, 0); PG8_STAGE(PG8_SA(0, 1), a2, va[1]);
;             PG8_WAIT_V(8); PG8_WAIT_L(0); PG8_BAR; PG8_MMA(0, 0, At, B0); PG8_MMA(0, 1, At, B1); PG8_BAR; PG8_SCHED;
	s_add_i32 s68, 0, 0x18000
	s_add_i32 s69, 0, 0x1c000
	v_add_u32_e32 v130, s68, v225
	v_add_u32_e32 v158, s69, v225
	ds_read_b128 v[118:121], v130
	ds_read_b128 v[122:125], v130 offset:1024
	ds_read_b128 v[126:129], v130 offset:2048
	ds_read_b128 v[130:133], v130 offset:3072
	ds_read_b128 v[146:149], v158
	ds_read_b128 v[150:153], v158 offset:1024
	ds_read_b128 v[154:157], v158 offset:2048
	ds_read_b128 v[158:161], v158 offset:3072
	s_mov_b32 m0, s44
	v_lshl_add_u64 v[218:219], s[36:37], 0, v[218:219]
	ds_read_b128 v[162:165], v228 offset:32768
	ds_read_b128 v[166:169], v228 offset:33792
	ds_read_b128 v[170:173], v228 offset:34816
	ds_read_b128 v[174:177], v228 offset:35840
	ds_read_b128 v[178:181], v228 offset:36864
	ds_read_b128 v[182:185], v228 offset:37888
	ds_read_b128 v[186:189], v228 offset:38912
	ds_read_b128 v[190:193], v228 offset:39936
	global_load_lds_dwordx4 v[218:219], off
	v_lshl_add_u64 v[216:217], s[36:37], 0, v[216:217]
	s_mov_b32 m0, s45
	s_nop 0
	global_load_lds_dwordx4 v[216:217], off
	s_waitcnt vmcnt(8)
	s_waitcnt lgkmcnt(0)
	s_barrier
	s_setprio 1
	s_waitcnt lgkmcnt(0)
	v_mfma_f32_16x16x32_bf16 v[142:145], v[118:121], v[162:165], v[142:145]
	v_mfma_f32_16x16x32_bf16 v[138:141], v[126:129], v[162:165], v[138:141]
	v_mfma_f32_16x16x32_bf16 v[110:113], v[118:121], v[170:173], v[110:113]
	v_mfma_f32_16x16x32_bf16 v[106:109], v[126:129], v[170:173], v[106:109]
	v_mfma_f32_16x16x32_bf16 v[94:97], v[118:121], v[178:181], v[94:97]
	v_mfma_f32_16x16x32_bf16 v[90:93], v[126:129], v[178:181], v[90:93]
	v_mfma_f32_16x16x32_bf16 v[78:81], v[118:121], v[186:189], v[78:81]
	v_mfma_f32_16x16x32_bf16 v[74:77], v[126:129], v[186:189], v[74:77]
	v_mfma_f32_16x16x32_bf16 v[142:145], v[122:125], v[166:169], v[142:145]
	v_mfma_f32_16x16x32_bf16 v[138:141], v[130:133], v[166:169], v[138:141]
	v_mfma_f32_16x16x32_bf16 v[110:113], v[122:125], v[174:177], v[110:113]
	v_mfma_f32_16x16x32_bf16 v[106:109], v[130:133], v[174:177], v[106:109]
	v_mfma_f32_16x16x32_bf16 v[94:97], v[122:125], v[182:185], v[94:97]
	v_mfma_f32_16x16x32_bf16 v[90:93], v[130:133], v[182:185], v[90:93]
	v_mfma_f32_16x16x32_bf16 v[78:81], v[122:125], v[190:193], v[78:81]
	v_mfma_f32_16x16x32_bf16 v[74:77], v[130:133], v[190:193], v[74:77]
	v_mfma_f32_16x16x32_bf16 v[134:137], v[146:149], v[162:165], v[134:137]
	v_mfma_f32_16x16x32_bf16 v[114:117], v[154:157], v[162:165], v[114:117]
	v_mfma_f32_16x16x32_bf16 v[102:105], v[146:149], v[170:173], v[102:105]
	v_mfma_f32_16x16x32_bf16 v[98:101], v[154:157], v[170:173], v[98:101]
	v_mfma_f32_16x16x32_bf16 v[86:89], v[146:149], v[178:181], v[86:89]
	v_mfma_f32_16x16x32_bf16 v[82:85], v[154:157], v[178:181], v[82:85]
	v_mfma_f32_16x16x32_bf16 v[70:73], v[146:149], v[186:189], v[70:73]
	v_mfma_f32_16x16x32_bf16 v[66:69], v[154:157], v[186:189], v[66:69]
	v_mfma_f32_16x16x32_bf16 v[134:137], v[150:153], v[166:169], v[134:137]
	v_mfma_f32_16x16x32_bf16 v[114:117], v[158:161], v[166:169], v[114:117]
	v_mfma_f32_16x16x32_bf16 v[102:105], v[150:153], v[174:177], v[102:105]
	v_mfma_f32_16x16x32_bf16 v[98:101], v[158:161], v[174:177], v[98:101]
	v_mfma_f32_16x16x32_bf16 v[86:89], v[150:153], v[182:185], v[86:89]
	v_mfma_f32_16x16x32_bf16 v[82:85], v[158:161], v[182:185], v[82:85]
	v_mfma_f32_16x16x32_bf16 v[70:73], v[150:153], v[190:193], v[70:73]
	v_mfma_f32_16x16x32_bf16 v[66:69], v[158:161], v[190:193], v[66:69]
	s_setprio 0
	s_barrier
; #define PG8_STAGE(bufoff, gbase, voff) do { _Pragma("unroll") for (int _i = 0; _i < 2; ++_i) \
;         __builtin_amdgcn_global_load_lds((const unsigned*)((const char*)(gbase) + (voff)[_i]), (LAS unsigned*)(lds + (bufoff) + ldsw + _i * 8192), 16, 0, 0); } while (0)
; #define PG8_LDA(dst, b, h) do { _Pragma("unroll") for (int m = 0; m < 4; ++m) _Pragma("unroll") for (int k = 0; k < 2; ++k) dst[m][k] = *(const LAS bf16x8*)(lds + PG8_SA(b, h) + aoff + m * 2048 + k * 1024); } while (0)
; #define PG8_WAIT_V(n) asm volatile("s_waitcnt vmcnt(" #n ")" ::: "memory")
; #define PG8_WAIT_L(n) asm volatile("s_waitcnt lgkmcnt(" #n ")" ::: "memory")
; #define PG8_BAR __builtin_amdgcn_s_barrier()
; #define PG8_SCHED __builtin_amdgcn_sched_barrier(0)
;     ...
;             PG8_LDA(At, 1, 1); PG8_STAGE(PG8_SB(1, 0), b3, voffB); PG8_STAGE(PG8_SB(1, 1), b3 + hstep, voffB); PG8_STAGE(PG8_SA(1, 0), a3, va[0]);
;             PG8_WAIT_V(8); PG8_WAIT_L(0); PG8_BAR; PG8_MMA(1, 0, At, B0); PG8_MMA(1, 1, At, B1); PG8_BAR; PG8_SCHED;
;         }
	s_add_i32 s36, s68, s3
	v_lshl_add_u64 v[216:217], v[232:233], 0, s[20:21]
	s_mov_b32 m0, s36
	ds_read_b128 v[162:165], v228 offset:49152
	ds_read_b128 v[166:169], v228 offset:50176
	ds_read_b128 v[170:173], v228 offset:51200
	ds_read_b128 v[174:177], v228 offset:52224
	ds_read_b128 v[178:181], v228 offset:53248
	ds_read_b128 v[182:185], v228 offset:54272
	ds_read_b128 v[186:189], v228 offset:55296
	ds_read_b128 v[190:193], v228 offset:56320
	global_load_lds_dwordx4 v[216:217], off
	s_add_i32 m0, s36, 0x2000
	s_add_u32 s34, s34, 0x80080
	v_lshl_add_u64 v[216:217], v[234:235], 0, s[20:21]
	s_addc_u32 s35, s35, 0
	s_add_i32 s36, s69, s3
	global_load_lds_dwordx4 v[216:217], off
	v_lshl_add_u64 v[216:217], s[34:35], 0, v[196:197]
	s_mov_b32 m0, s36
	s_nop 0
	global_load_lds_dwordx4 v[216:217], off
	v_lshl_add_u64 v[216:217], s[34:35], 0, v[198:199]
	s_add_i32 m0, s36, 0x2000
	s_nop 0
	global_load_lds_dwordx4 v[216:217], off
	v_lshl_add_u64 v[216:217], v[236:237], 0, s[20:21]
	s_mov_b32 m0, s49
	s_nop 0
	global_load_lds_dwordx4 v[216:217], off
	v_lshl_add_u64 v[216:217], v[238:239], 0, s[20:21]
	s_mov_b32 m0, s51
	s_nop 0
	global_load_lds_dwordx4 v[216:217], off
	s_waitcnt vmcnt(8)
	s_waitcnt lgkmcnt(0)
	s_barrier
	s_setprio 1
	s_waitcnt lgkmcnt(0)
	v_mfma_f32_16x16x32_bf16 v[62:65], v[118:121], v[162:165], v[62:65]
	v_mfma_f32_16x16x32_bf16 v[58:61], v[126:129], v[162:165], v[58:61]
	v_mfma_f32_16x16x32_bf16 v[46:49], v[118:121], v[170:173], v[46:49]
	v_mfma_f32_16x16x32_bf16 v[42:45], v[126:129], v[170:173], v[42:45]
	v_mfma_f32_16x16x32_bf16 v[30:33], v[118:121], v[178:181], v[30:33]
	v_mfma_f32_16x16x32_bf16 v[26:29], v[126:129], v[178:181], v[26:29]
	v_mfma_f32_16x16x32_bf16 v[14:17], v[118:121], v[186:189], v[14:17]
	v_mfma_f32_16x16x32_bf16 v[10:13], v[126:129], v[186:189], v[10:13]
	v_mfma_f32_16x16x32_bf16 v[62:65], v[122:125], v[166:169], v[62:65]
	v_mfma_f32_16x16x32_bf16 v[58:61], v[130:133], v[166:169], v[58:61]
	v_mfma_f32_16x16x32_bf16 v[46:49], v[122:125], v[174:177], v[46:49]
	v_mfma_f32_16x16x32_bf16 v[42:45], v[130:133], v[174:177], v[42:45]
	v_mfma_f32_16x16x32_bf16 v[30:33], v[122:125], v[182:185], v[30:33]
	v_mfma_f32_16x16x32_bf16 v[26:29], v[130:133], v[182:185], v[26:29]
	v_mfma_f32_16x16x32_bf16 v[14:17], v[122:125], v[190:193], v[14:17]
	v_mfma_f32_16x16x32_bf16 v[10:13], v[130:133], v[190:193], v[10:13]
	v_mfma_f32_16x16x32_bf16 v[54:57], v[146:149], v[162:165], v[54:57]
	v_mfma_f32_16x16x32_bf16 v[50:53], v[154:157], v[162:165], v[50:53]
	v_mfma_f32_16x16x32_bf16 v[38:41], v[146:149], v[170:173], v[38:41]
	v_mfma_f32_16x16x32_bf16 v[34:37], v[154:157], v[170:173], v[34:37]
	v_mfma_f32_16x16x32_bf16 v[22:25], v[146:149], v[178:181], v[22:25]
	v_mfma_f32_16x16x32_bf16 v[18:21], v[154:157], v[178:181], v[18:21]
	v_mfma_f32_16x16x32_bf16 v[6:9], v[146:149], v[186:189], v[6:9]
	v_mfma_f32_16x16x32_bf16 v[2:5], v[154:157], v[186:189], v[2:5]
	v_mfma_f32_16x16x32_bf16 v[54:57], v[150:153], v[166:169], v[54:57]
	v_mfma_f32_16x16x32_bf16 v[50:53], v[158:161], v[166:169], v[50:53]
	v_mfma_f32_16x16x32_bf16 v[38:41], v[150:153], v[174:177], v[38:41]
	v_mfma_f32_16x16x32_bf16 v[34:37], v[158:161], v[174:177], v[34:37]
	v_mfma_f32_16x16x32_bf16 v[22:25], v[150:153], v[182:185], v[22:25]
	v_mfma_f32_16x16x32_bf16 v[18:21], v[158:161], v[182:185], v[18:21]
	v_mfma_f32_16x16x32_bf16 v[6:9], v[150:153], v[190:193], v[6:9]
	v_mfma_f32_16x16x32_bf16 v[2:5], v[158:161], v[190:193], v[2:5]
	s_setprio 0
	s_barrier
	s_add_i32 s63, s63, 2
	s_add_u32 s57, s57, 0x100
	s_addc_u32 s62, s62, 0
	s_add_u32 s8, s8, 0x100
	s_addc_u32 s9, s9, 0
	s_cmp_gt_u32 s63, 29
	s_cbranch_scc1 .LBB0_685

; #define PG8_STAGE(bufoff, gbase, voff) do { _Pragma("unroll") for (int _i = 0; _i < 2; ++_i) \
;         __builtin_amdgcn_global_load_lds((const unsigned*)((const char*)(gbase) + (voff)[_i]), (LAS unsigned*)(lds + (bufoff) + ldsw + _i * 8192), 16, 0, 0); } while (0)
; #define PG8_LDA(dst, b, h) do { _Pragma("unroll") for (int m = 0; m < 4; ++m) _Pragma("unroll") for (int k = 0; k < 2; ++k) dst[m][k] = *(const LAS bf16x8*)(lds + PG8_SA(b, h) + aoff + m * 2048 + k * 1024); } while (0)
; #define PG8_LDB(dst, b, h) do { _Pragma("unroll") for (int n = 0; n < 2; ++n) _Pragma("unroll") for (int k = 0; k < 2; ++k) dst[n][k] = *(const LAS bf16x8*)(lds + PG8_SB(b, h) + boff + n * 2048 + k * 1024); } while (0)
; #define PG8_WAIT_V(n) asm volatile("s_waitcnt vmcnt(" #n ")" ::: "memory")
; #define PG8_WAIT_L(n) asm volatile("s_waitcnt lgkmcnt(" #n ")" ::: "memory")
; #define PG8_BAR __builtin_amdgcn_s_barrier()
; #define PG8_SCHED __builtin_amdgcn_sched_barrier(0)
;     ...
;             const bool last = (t == nt - 2);
;             const char* a1 = cA + (size_t)(t + 1) * kstep;
;             const char* a2 = last ? cA : cA + (size_t)(t + 2) * kstep; const char* b2 = last ? nB : cB + (size_t)(t + 2) * kstep;
;             const char* a3 = a2 + kstep; const char* b3 = b2 + kstep;
;             PG8_LDB(B0, 0, 0); PG8_LDB(B1, 0, 1); PG8_SCHED; PG8_LDA(At, 0, 0); PG8_STAGE(PG8_SA(1, 1), a1, va[1]);
;             if (last) {
; #pragma unroll
;                 for (int h = 0; h < 2; ++h)
; #pragma unroll
;                     for (int i = 0; i < 2; ++i) va[h][i] = vn[h][i]; }
;             PG8_WAIT_V(8); PG8_WAIT_L(0); PG8_BAR; PG8_MMA(0, 0, At, B0); PG8_MMA(0, 1, At, B1); PG8_BAR; PG8_SCHED;
;             PG8_LDA(At, 0, 1); PG8_STAGE(PG8_SB(0, 0), b2, voffB); PG8_STAGE(PG8_SB(0, 1), b2 + hstep, voffB); PG8_STAGE(PG8_SA(0, 0), a2, va[0]);
;             PG8_WAIT_V(8); PG8_WAIT_L(0); PG8_BAR; PG8_MMA(1, 0, At, B0); PG8_MMA(1, 1, At, B1); PG8_BAR; PG8_SCHED;
.LBB0_1035:
	s_waitcnt vmcnt(8)
	s_add_u32 s54, s48, 0x80
	s_waitcnt lgkmcnt(0)
	s_addc_u32 s55, s49, 0
	s_and_b64 s[52:53], s[52:53], exec
	s_cselect_b32 s55, s27, s55
	s_cselect_b32 s54, s26, s54
	s_cselect_b32 s53, s47, s45
	s_cselect_b32 s52, s46, s43
	s_barrier
	s_setprio 1
	s_waitcnt lgkmcnt(0)
	v_mfma_scale_f32_16x16x128_f8f6f4 v[190:193], v[18:25], v[58:65], v[190:193], v227, v226 op_sel_hi:[0,0,0]
	v_mfma_scale_f32_16x16x128_f8f6f4 v[182:185], v[26:33], v[58:65], v[182:185], v227, v226 op_sel_hi:[0,0,0]
	v_mfma_scale_f32_16x16x128_f8f6f4 v[174:177], v[18:25], v[50:57], v[174:177], v227, v226 op_sel_hi:[0,0,0]
	v_mfma_scale_f32_16x16x128_f8f6f4 v[166:169], v[26:33], v[50:57], v[166:169], v227, v226 op_sel_hi:[0,0,0]
	v_mfma_scale_f32_16x16x128_f8f6f4 v[158:161], v[18:25], v[42:49], v[158:161], v227, v226 op_sel_hi:[0,0,0]
	v_mfma_scale_f32_16x16x128_f8f6f4 v[150:153], v[26:33], v[42:49], v[150:153], v227, v226 op_sel_hi:[0,0,0]
	v_mfma_scale_f32_16x16x128_f8f6f4 v[142:145], v[18:25], v[34:41], v[142:145], v227, v226 op_sel_hi:[0,0,0]
	v_mfma_scale_f32_16x16x128_f8f6f4 v[134:137], v[26:33], v[34:41], v[134:137], v227, v226 op_sel_hi:[0,0,0]
	v_mfma_scale_f32_16x16x128_f8f6f4 v[186:189], v[2:9], v[58:65], v[186:189], v227, v226 op_sel_hi:[0,0,0]
	v_mfma_scale_f32_16x16x128_f8f6f4 v[178:181], v[10:17], v[58:65], v[178:181], v227, v226 op_sel_hi:[0,0,0]
	v_mfma_scale_f32_16x16x128_f8f6f4 v[170:173], v[2:9], v[50:57], v[170:173], v227, v226 op_sel_hi:[0,0,0]
	v_mfma_scale_f32_16x16x128_f8f6f4 v[162:165], v[10:17], v[50:57], v[162:165], v227, v226 op_sel_hi:[0,0,0]
	v_mfma_scale_f32_16x16x128_f8f6f4 v[154:157], v[2:9], v[42:49], v[154:157], v227, v226 op_sel_hi:[0,0,0]
	v_mfma_scale_f32_16x16x128_f8f6f4 v[146:149], v[10:17], v[42:49], v[146:149], v227, v226 op_sel_hi:[0,0,0]
	v_mfma_scale_f32_16x16x128_f8f6f4 v[138:141], v[2:9], v[34:41], v[138:141], v227, v226 op_sel_hi:[0,0,0]
	v_mfma_scale_f32_16x16x128_f8f6f4 v[130:133], v[10:17], v[34:41], v[130:133], v227, v226 op_sel_hi:[0,0,0]
	s_setprio 0
	s_barrier
	s_mov_b32 m0, s37
	v_lshl_add_u64 v[232:233], s[52:53], 0, v[196:197]
	s_add_u32 s72, s52, 0x40000
	ds_read_b128 v[34:37], v225 offset:16384
	ds_read_b128 v[38:41], v225 offset:17408
	ds_read_b128 v[42:45], v225 offset:18432
	ds_read_b128 v[46:49], v225 offset:19456
	ds_read_b128 v[50:53], v225 offset:20480
	ds_read_b128 v[54:57], v225 offset:21504
	ds_read_b128 v[58:61], v225 offset:22528
	ds_read_b128 v[62:65], v225 offset:23552
	global_load_lds_dwordx4 v[232:233], off
	v_lshl_add_u64 v[234:235], s[52:53], 0, v[198:199]
	s_mov_b32 m0, s39
	s_addc_u32 s73, s53, 0
	global_load_lds_dwordx4 v[234:235], off
	v_lshl_add_u64 v[236:237], s[72:73], 0, v[196:197]
	s_mov_b32 m0, s41
	v_mov_b32_e32 v205, v201
	global_load_lds_dwordx4 v[236:237], off
	v_lshl_add_u64 v[236:237], s[72:73], 0, v[198:199]
	s_mov_b32 m0, s56
	v_lshl_add_u64 v[238:239], s[54:55], 0, v[204:205]
	global_load_lds_dwordx4 v[236:237], off
	s_mov_b32 m0, s35
	v_lshl_add_u64 v[236:237], s[54:55], 0, v[200:201]
	global_load_lds_dwordx4 v200, s[54:55]
	s_mov_b32 m0, s57
	s_nop 0
	global_load_lds_dwordx4 v204, s[54:55]
	s_waitcnt vmcnt(8)
	s_waitcnt lgkmcnt(0)
	s_barrier
	s_setprio 1
	s_waitcnt lgkmcnt(0)
	v_mfma_scale_f32_16x16x128_f8f6f4 v[126:129], v[18:25], v[34:41], v[126:129], v227, v226 op_sel_hi:[0,0,0]
	v_mfma_scale_f32_16x16x128_f8f6f4 v[118:121], v[26:33], v[34:41], v[118:121], v227, v226 op_sel_hi:[0,0,0]
	v_mfma_scale_f32_16x16x128_f8f6f4 v[110:113], v[18:25], v[42:49], v[110:113], v227, v226 op_sel_hi:[0,0,0]
	v_mfma_scale_f32_16x16x128_f8f6f4 v[102:105], v[26:33], v[42:49], v[102:105], v227, v226 op_sel_hi:[0,0,0]
	v_mfma_scale_f32_16x16x128_f8f6f4 v[94:97], v[18:25], v[50:57], v[94:97], v227, v226 op_sel_hi:[0,0,0]
	v_mfma_scale_f32_16x16x128_f8f6f4 v[86:89], v[26:33], v[50:57], v[86:89], v227, v226 op_sel_hi:[0,0,0]
	v_mfma_scale_f32_16x16x128_f8f6f4 v[78:81], v[18:25], v[58:65], v[78:81], v227, v226 op_sel_hi:[0,0,0]
	v_mfma_scale_f32_16x16x128_f8f6f4 v[70:73], v[26:33], v[58:65], v[70:73], v227, v226 op_sel_hi:[0,0,0]
	v_mfma_scale_f32_16x16x128_f8f6f4 v[122:125], v[2:9], v[34:41], v[122:125], v227, v226 op_sel_hi:[0,0,0]
	v_mfma_scale_f32_16x16x128_f8f6f4 v[114:117], v[10:17], v[34:41], v[114:117], v227, v226 op_sel_hi:[0,0,0]
	v_mfma_scale_f32_16x16x128_f8f6f4 v[106:109], v[2:9], v[42:49], v[106:109], v227, v226 op_sel_hi:[0,0,0]
	v_mfma_scale_f32_16x16x128_f8f6f4 v[98:101], v[10:17], v[42:49], v[98:101], v227, v226 op_sel_hi:[0,0,0]
	v_mfma_scale_f32_16x16x128_f8f6f4 v[90:93], v[2:9], v[50:57], v[90:93], v227, v226 op_sel_hi:[0,0,0]
	v_mfma_scale_f32_16x16x128_f8f6f4 v[82:85], v[10:17], v[50:57], v[82:85], v227, v226 op_sel_hi:[0,0,0]
	v_mfma_scale_f32_16x16x128_f8f6f4 v[74:77], v[2:9], v[58:65], v[74:77], v227, v226 op_sel_hi:[0,0,0]
	v_mfma_scale_f32_16x16x128_f8f6f4 v[66:69], v[10:17], v[58:65], v[66:69], v227, v226 op_sel_hi:[0,0,0]
	s_setprio 0
	s_barrier
; #define PG8_STAGE(bufoff, gbase, voff) do { _Pragma("unroll") for (int _i = 0; _i < 2; ++_i) \
;         __builtin_amdgcn_global_load_lds((const unsigned*)((const char*)(gbase) + (voff)[_i]), (LAS unsigned*)(lds + (bufoff) + ldsw + _i * 8192), 16, 0, 0); } while (0)
; #define PG8_LDA(dst, b, h) do { _Pragma("unroll") for (int m = 0; m < 4; ++m) _Pragma("unroll") for (int k = 0; k < 2; ++k) dst[m][k] = *(const LAS bf16x8*)(lds + PG8_SA(b, h) + aoff + m * 2048 + k * 1024); } while (0)
; #define PG8_LDB(dst, b, h) do { _Pragma("unroll") for (int n = 0; n < 2; ++n) _Pragma("unroll") for (int k = 0; k < 2; ++k) dst[n][k] = *(const LAS bf16x8*)(lds + PG8_SB(b, h) + boff + n * 2048 + k * 1024); } while (0)
; #define PG8_WAIT_V(n) asm volatile("s_waitcnt vmcnt(" #n ")" ::: "memory")
; #define PG8_WAIT_L(n) asm volatile("s_waitcnt lgkmcnt(" #n ")" ::: "memory")
; #define PG8_BAR __builtin_amdgcn_s_barrier()
; #define PG8_SCHED __builtin_amdgcn_sched_barrier(0)
;     ...
;             PG8_LDB(B0, 1, 0); PG8_LDB(B1, 1, 1); PG8_SCHED; PG8_LDA(At, 1, 0); PG8_STAGE(PG8_SA(0, 1), a2, va[1]);
;             PG8_WAIT_V(8); PG8_WAIT_L(0); PG8_BAR; PG8_MMA(0, 0, At, B0); PG8_MMA(0, 1, At, B1); PG8_BAR; PG8_SCHED;
;             PG8_LDA(At, 1, 1); PG8_STAGE(PG8_SB(1, 0), b3, voffB); PG8_STAGE(PG8_SB(1, 1), b3 + hstep, voffB); PG8_STAGE(PG8_SA(1, 0), a3, va[0]);
;             PG8_WAIT_V(8); PG8_WAIT_L(0); PG8_BAR; PG8_MMA(1, 0, At, B0); PG8_MMA(1, 1, At, B1); PG8_BAR; PG8_SCHED;
;         }
	s_add_i32 s71, 0, 0x18000
	s_add_i32 s72, 0, 0x1c000
	v_add_u32_e32 v14, s71, v219
	v_add_u32_e32 v30, s72, v219
	ds_read_b128 v[2:5], v14
	ds_read_b128 v[6:9], v14 offset:1024
	ds_read_b128 v[10:13], v14 offset:2048
	ds_read_b128 v[14:17], v14 offset:3072
	ds_read_b128 v[18:21], v30
	ds_read_b128 v[22:25], v30 offset:1024
	ds_read_b128 v[26:29], v30 offset:2048
	ds_read_b128 v[30:33], v30 offset:3072
	s_mov_b32 m0, s59
	v_lshl_add_u64 v[214:215], s[54:55], 0, v[214:215]
	ds_read_b128 v[34:37], v225 offset:32768
	ds_read_b128 v[38:41], v225 offset:33792
	ds_read_b128 v[42:45], v225 offset:34816
	ds_read_b128 v[46:49], v225 offset:35840
	ds_read_b128 v[50:53], v225 offset:36864
	ds_read_b128 v[54:57], v225 offset:37888
	ds_read_b128 v[58:61], v225 offset:38912
	ds_read_b128 v[62:65], v225 offset:39936
	global_load_lds_dwordx4 v[214:215], off
	v_lshl_add_u64 v[212:213], s[54:55], 0, v[212:213]
	s_mov_b32 m0, s60
	s_nop 0
	global_load_lds_dwordx4 v[212:213], off
	s_waitcnt vmcnt(8)
	s_waitcnt lgkmcnt(0)
	s_barrier
	s_setprio 1
	s_waitcnt lgkmcnt(0)
	v_mfma_scale_f32_16x16x128_f8f6f4 v[190:193], v[2:9], v[34:41], v[190:193], v227, v226 op_sel_hi:[0,0,0]
	v_mfma_scale_f32_16x16x128_f8f6f4 v[182:185], v[10:17], v[34:41], v[182:185], v227, v226 op_sel_hi:[0,0,0]
	v_mfma_scale_f32_16x16x128_f8f6f4 v[174:177], v[2:9], v[42:49], v[174:177], v227, v226 op_sel_hi:[0,0,0]
	v_mfma_scale_f32_16x16x128_f8f6f4 v[166:169], v[10:17], v[42:49], v[166:169], v227, v226 op_sel_hi:[0,0,0]
	v_mfma_scale_f32_16x16x128_f8f6f4 v[158:161], v[2:9], v[50:57], v[158:161], v227, v226 op_sel_hi:[0,0,0]
	v_mfma_scale_f32_16x16x128_f8f6f4 v[150:153], v[10:17], v[50:57], v[150:153], v227, v226 op_sel_hi:[0,0,0]
	v_mfma_scale_f32_16x16x128_f8f6f4 v[142:145], v[2:9], v[58:65], v[142:145], v227, v226 op_sel_hi:[0,0,0]
	v_mfma_scale_f32_16x16x128_f8f6f4 v[134:137], v[10:17], v[58:65], v[134:137], v227, v226 op_sel_hi:[0,0,0]
	v_mfma_scale_f32_16x16x128_f8f6f4 v[186:189], v[18:25], v[34:41], v[186:189], v227, v226 op_sel_hi:[0,0,0]
	v_mfma_scale_f32_16x16x128_f8f6f4 v[178:181], v[26:33], v[34:41], v[178:181], v227, v226 op_sel_hi:[0,0,0]
	v_mfma_scale_f32_16x16x128_f8f6f4 v[170:173], v[18:25], v[42:49], v[170:173], v227, v226 op_sel_hi:[0,0,0]
	v_mfma_scale_f32_16x16x128_f8f6f4 v[162:165], v[26:33], v[42:49], v[162:165], v227, v226 op_sel_hi:[0,0,0]
	v_mfma_scale_f32_16x16x128_f8f6f4 v[154:157], v[18:25], v[50:57], v[154:157], v227, v226 op_sel_hi:[0,0,0]
	v_mfma_scale_f32_16x16x128_f8f6f4 v[146:149], v[26:33], v[50:57], v[146:149], v227, v226 op_sel_hi:[0,0,0]
	v_mfma_scale_f32_16x16x128_f8f6f4 v[138:141], v[18:25], v[58:65], v[138:141], v227, v226 op_sel_hi:[0,0,0]
	v_mfma_scale_f32_16x16x128_f8f6f4 v[130:133], v[26:33], v[58:65], v[130:133], v227, v226 op_sel_hi:[0,0,0]
	s_setprio 0
	s_barrier
	s_add_i32 s54, s71, s2
	v_lshl_add_u64 v[212:213], v[232:233], 0, s[14:15]
	s_mov_b32 m0, s54
	ds_read_b128 v[34:37], v225 offset:49152
	ds_read_b128 v[38:41], v225 offset:50176
	ds_read_b128 v[42:45], v225 offset:51200
	ds_read_b128 v[46:49], v225 offset:52224
	ds_read_b128 v[50:53], v225 offset:53248
	ds_read_b128 v[54:57], v225 offset:54272
	ds_read_b128 v[58:61], v225 offset:55296
	ds_read_b128 v[62:65], v225 offset:56320
	global_load_lds_dwordx4 v[212:213], off
	s_add_i32 m0, s54, 0x2000
	s_add_u32 s52, s52, 0x40080
	v_lshl_add_u64 v[212:213], v[234:235], 0, s[14:15]
	s_addc_u32 s53, s53, 0
	s_add_i32 s54, s72, s2
	global_load_lds_dwordx4 v[212:213], off
	v_lshl_add_u64 v[212:213], s[52:53], 0, v[196:197]
	s_mov_b32 m0, s54
	s_nop 0
	global_load_lds_dwordx4 v[212:213], off
	v_lshl_add_u64 v[212:213], s[52:53], 0, v[198:199]
	s_add_i32 m0, s54, 0x2000
	s_nop 0
	global_load_lds_dwordx4 v[212:213], off
	v_lshl_add_u64 v[212:213], v[236:237], 0, s[14:15]
	s_mov_b32 m0, s62
	s_nop 0
	global_load_lds_dwordx4 v[212:213], off
	v_lshl_add_u64 v[212:213], v[238:239], 0, s[14:15]
	s_mov_b32 m0, s63
	s_nop 0
	global_load_lds_dwordx4 v[212:213], off
	s_waitcnt vmcnt(8)
	s_waitcnt lgkmcnt(0)
	s_barrier
	s_setprio 1
	s_waitcnt lgkmcnt(0)
	v_mfma_scale_f32_16x16x128_f8f6f4 v[126:129], v[2:9], v[34:41], v[126:129], v227, v226 op_sel_hi:[0,0,0]
	v_mfma_scale_f32_16x16x128_f8f6f4 v[118:121], v[10:17], v[34:41], v[118:121], v227, v226 op_sel_hi:[0,0,0]
	v_mfma_scale_f32_16x16x128_f8f6f4 v[110:113], v[2:9], v[42:49], v[110:113], v227, v226 op_sel_hi:[0,0,0]
	v_mfma_scale_f32_16x16x128_f8f6f4 v[102:105], v[10:17], v[42:49], v[102:105], v227, v226 op_sel_hi:[0,0,0]
	v_mfma_scale_f32_16x16x128_f8f6f4 v[94:97], v[2:9], v[50:57], v[94:97], v227, v226 op_sel_hi:[0,0,0]
	v_mfma_scale_f32_16x16x128_f8f6f4 v[86:89], v[10:17], v[50:57], v[86:89], v227, v226 op_sel_hi:[0,0,0]
	v_mfma_scale_f32_16x16x128_f8f6f4 v[78:81], v[2:9], v[58:65], v[78:81], v227, v226 op_sel_hi:[0,0,0]
	v_mfma_scale_f32_16x16x128_f8f6f4 v[70:73], v[10:17], v[58:65], v[70:73], v227, v226 op_sel_hi:[0,0,0]
	v_mfma_scale_f32_16x16x128_f8f6f4 v[122:125], v[18:25], v[34:41], v[122:125], v227, v226 op_sel_hi:[0,0,0]
	v_mfma_scale_f32_16x16x128_f8f6f4 v[114:117], v[26:33], v[34:41], v[114:117], v227, v226 op_sel_hi:[0,0,0]
	v_mfma_scale_f32_16x16x128_f8f6f4 v[106:109], v[18:25], v[42:49], v[106:109], v227, v226 op_sel_hi:[0,0,0]
	v_mfma_scale_f32_16x16x128_f8f6f4 v[98:101], v[26:33], v[42:49], v[98:101], v227, v226 op_sel_hi:[0,0,0]
	v_mfma_scale_f32_16x16x128_f8f6f4 v[90:93], v[18:25], v[50:57], v[90:93], v227, v226 op_sel_hi:[0,0,0]
	v_mfma_scale_f32_16x16x128_f8f6f4 v[82:85], v[26:33], v[50:57], v[82:85], v227, v226 op_sel_hi:[0,0,0]
	v_mfma_scale_f32_16x16x128_f8f6f4 v[74:77], v[18:25], v[58:65], v[74:77], v227, v226 op_sel_hi:[0,0,0]
	v_mfma_scale_f32_16x16x128_f8f6f4 v[66:69], v[26:33], v[58:65], v[66:69], v227, v226 op_sel_hi:[0,0,0]
	s_setprio 0
	s_barrier
	s_add_i32 s70, s70, 2
	s_add_u32 s43, s43, 0x100
	s_addc_u32 s45, s45, 0
	s_add_u32 s48, s48, 0x100
	s_addc_u32 s49, s49, 0
	s_cmp_gt_u32 s70, 13
	s_cbranch_scc1 .LBB0_1038

; #define PG8_STAGE(bufoff, gbase, voff) do { _Pragma("unroll") for (int _i = 0; _i < 2; ++_i) \
;         __builtin_amdgcn_global_load_lds((const unsigned*)((const char*)(gbase) + (voff)[_i]), (LAS unsigned*)(lds + (bufoff) + ldsw + _i * 8192), 16, 0, 0); } while (0)
; #define PG8_LDA(dst, b, h) do { _Pragma("unroll") for (int m = 0; m < 4; ++m) _Pragma("unroll") for (int k = 0; k < 2; ++k) dst[m][k] = *(const LAS bf16x8*)(lds + PG8_SA(b, h) + aoff + m * 2048 + k * 1024); } while (0)
; #define PG8_LDB(dst, b, h) do { _Pragma("unroll") for (int n = 0; n < 2; ++n) _Pragma("unroll") for (int k = 0; k < 2; ++k) dst[n][k] = *(const LAS bf16x8*)(lds + PG8_SB(b, h) + boff + n * 2048 + k * 1024); } while (0)
; #define PG8_WAIT_V(n) asm volatile("s_waitcnt vmcnt(" #n ")" ::: "memory")
; #define PG8_WAIT_L(n) asm volatile("s_waitcnt lgkmcnt(" #n ")" ::: "memory")
; #define PG8_BAR __builtin_amdgcn_s_barrier()
; #define PG8_SCHED __builtin_amdgcn_sched_barrier(0)
;     ...
;             const bool last = (t == nt - 2);
;             const char* a1 = cA + (size_t)(t + 1) * kstep;
;             const char* a2 = last ? cA : cA + (size_t)(t + 2) * kstep; const char* b2 = last ? nB : cB + (size_t)(t + 2) * kstep;
;             const char* a3 = a2 + kstep; const char* b3 = b2 + kstep;
;             PG8_LDB(B0, 0, 0); PG8_LDB(B1, 0, 1); PG8_SCHED; PG8_LDA(At, 0, 0); PG8_STAGE(PG8_SA(1, 1), a1, va[1]);
;             if (last) {
; #pragma unroll
;                 for (int h = 0; h < 2; ++h)
; #pragma unroll
;                     for (int i = 0; i < 2; ++i) va[h][i] = vn[h][i]; }
;             PG8_WAIT_V(8); PG8_WAIT_L(0); PG8_BAR; PG8_MMA(0, 0, At, B0); PG8_MMA(0, 1, At, B1); PG8_BAR; PG8_SCHED;
;             PG8_LDA(At, 0, 1); PG8_STAGE(PG8_SB(0, 0), b2, voffB); PG8_STAGE(PG8_SB(0, 1), b2 + hstep, voffB); PG8_STAGE(PG8_SA(0, 0), a2, va[0]);
;             PG8_WAIT_V(8); PG8_WAIT_L(0); PG8_BAR; PG8_MMA(1, 0, At, B0); PG8_MMA(1, 1, At, B1); PG8_BAR; PG8_SCHED;
.LBB0_1187:
	s_waitcnt vmcnt(8)
	s_add_u32 s38, s34, 0x80
	s_waitcnt lgkmcnt(0)
	s_addc_u32 s39, s35, 0
	s_and_b64 s[36:37], s[36:37], exec
	s_cselect_b32 s39, s17, s39
	s_cselect_b32 s38, s16, s38
	s_cselect_b32 s37, s31, s29
	s_cselect_b32 s36, s30, s27
	s_barrier
	s_setprio 1
	s_waitcnt lgkmcnt(0)
	v_mfma_scale_f32_16x16x128_f8f6f4 v[190:193], v[18:25], v[58:65], v[190:193], v227, v226 op_sel_hi:[0,0,0]
	v_mfma_scale_f32_16x16x128_f8f6f4 v[186:189], v[26:33], v[58:65], v[186:189], v227, v226 op_sel_hi:[0,0,0]
	v_mfma_scale_f32_16x16x128_f8f6f4 v[182:185], v[18:25], v[50:57], v[182:185], v227, v226 op_sel_hi:[0,0,0]
	v_mfma_scale_f32_16x16x128_f8f6f4 v[178:181], v[26:33], v[50:57], v[178:181], v227, v226 op_sel_hi:[0,0,0]
	v_mfma_scale_f32_16x16x128_f8f6f4 v[158:161], v[18:25], v[42:49], v[158:161], v227, v226 op_sel_hi:[0,0,0]
	v_mfma_scale_f32_16x16x128_f8f6f4 v[154:157], v[26:33], v[42:49], v[154:157], v227, v226 op_sel_hi:[0,0,0]
	v_mfma_scale_f32_16x16x128_f8f6f4 v[150:153], v[18:25], v[34:41], v[150:153], v227, v226 op_sel_hi:[0,0,0]
	v_mfma_scale_f32_16x16x128_f8f6f4 v[146:149], v[26:33], v[34:41], v[146:149], v227, v226 op_sel_hi:[0,0,0]
	v_mfma_scale_f32_16x16x128_f8f6f4 v[174:177], v[2:9], v[58:65], v[174:177], v227, v226 op_sel_hi:[0,0,0]
	v_mfma_scale_f32_16x16x128_f8f6f4 v[170:173], v[10:17], v[58:65], v[170:173], v227, v226 op_sel_hi:[0,0,0]
	v_mfma_scale_f32_16x16x128_f8f6f4 v[166:169], v[2:9], v[50:57], v[166:169], v227, v226 op_sel_hi:[0,0,0]
	v_mfma_scale_f32_16x16x128_f8f6f4 v[162:165], v[10:17], v[50:57], v[162:165], v227, v226 op_sel_hi:[0,0,0]
	v_mfma_scale_f32_16x16x128_f8f6f4 v[142:145], v[2:9], v[42:49], v[142:145], v227, v226 op_sel_hi:[0,0,0]
	v_mfma_scale_f32_16x16x128_f8f6f4 v[138:141], v[10:17], v[42:49], v[138:141], v227, v226 op_sel_hi:[0,0,0]
	v_mfma_scale_f32_16x16x128_f8f6f4 v[134:137], v[2:9], v[34:41], v[134:137], v227, v226 op_sel_hi:[0,0,0]
	v_mfma_scale_f32_16x16x128_f8f6f4 v[130:133], v[10:17], v[34:41], v[130:133], v227, v226 op_sel_hi:[0,0,0]
	s_setprio 0
	s_barrier
	s_mov_b32 m0, s25
	v_lshl_add_u64 v[230:231], s[36:37], 0, v[198:199]
	s_add_u32 s64, s36, 0x40000
	ds_read_b128 v[34:37], v225 offset:16384
	ds_read_b128 v[38:41], v225 offset:17408
	ds_read_b128 v[42:45], v225 offset:18432
	ds_read_b128 v[46:49], v225 offset:19456
	ds_read_b128 v[50:53], v225 offset:20480
	ds_read_b128 v[54:57], v225 offset:21504
	ds_read_b128 v[58:61], v225 offset:22528
	ds_read_b128 v[62:65], v225 offset:23552
	global_load_lds_dwordx4 v[230:231], off
	v_lshl_add_u64 v[232:233], s[36:37], 0, v[196:197]
	s_mov_b32 m0, s33
	s_addc_u32 s65, s37, 0
	global_load_lds_dwordx4 v[232:233], off
	v_lshl_add_u64 v[234:235], s[64:65], 0, v[198:199]
	s_mov_b32 m0, s40
	v_mov_b32_e32 v207, v201
	global_load_lds_dwordx4 v[234:235], off
	v_lshl_add_u64 v[234:235], s[64:65], 0, v[196:197]
	s_mov_b32 m0, s41
	v_lshl_add_u64 v[236:237], s[38:39], 0, v[206:207]
	global_load_lds_dwordx4 v[234:235], off
	s_mov_b32 m0, s3
	v_lshl_add_u64 v[234:235], s[38:39], 0, v[200:201]
	global_load_lds_dwordx4 v200, s[38:39]
	s_mov_b32 m0, s42
	s_nop 0
	global_load_lds_dwordx4 v206, s[38:39]
	s_waitcnt vmcnt(8)
	s_waitcnt lgkmcnt(0)
	s_barrier
	s_setprio 1
	s_waitcnt lgkmcnt(0)
	v_mfma_scale_f32_16x16x128_f8f6f4 v[126:129], v[18:25], v[34:41], v[126:129], v227, v226 op_sel_hi:[0,0,0]
	v_mfma_scale_f32_16x16x128_f8f6f4 v[122:125], v[26:33], v[34:41], v[122:125], v227, v226 op_sel_hi:[0,0,0]
	v_mfma_scale_f32_16x16x128_f8f6f4 v[118:121], v[18:25], v[42:49], v[118:121], v227, v226 op_sel_hi:[0,0,0]
	v_mfma_scale_f32_16x16x128_f8f6f4 v[114:117], v[26:33], v[42:49], v[114:117], v227, v226 op_sel_hi:[0,0,0]
	v_mfma_scale_f32_16x16x128_f8f6f4 v[94:97], v[18:25], v[50:57], v[94:97], v227, v226 op_sel_hi:[0,0,0]
	v_mfma_scale_f32_16x16x128_f8f6f4 v[90:93], v[26:33], v[50:57], v[90:93], v227, v226 op_sel_hi:[0,0,0]
	v_mfma_scale_f32_16x16x128_f8f6f4 v[86:89], v[18:25], v[58:65], v[86:89], v227, v226 op_sel_hi:[0,0,0]
	v_mfma_scale_f32_16x16x128_f8f6f4 v[82:85], v[26:33], v[58:65], v[82:85], v227, v226 op_sel_hi:[0,0,0]
	v_mfma_scale_f32_16x16x128_f8f6f4 v[110:113], v[2:9], v[34:41], v[110:113], v227, v226 op_sel_hi:[0,0,0]
	v_mfma_scale_f32_16x16x128_f8f6f4 v[106:109], v[10:17], v[34:41], v[106:109], v227, v226 op_sel_hi:[0,0,0]
	v_mfma_scale_f32_16x16x128_f8f6f4 v[102:105], v[2:9], v[42:49], v[102:105], v227, v226 op_sel_hi:[0,0,0]
	v_mfma_scale_f32_16x16x128_f8f6f4 v[98:101], v[10:17], v[42:49], v[98:101], v227, v226 op_sel_hi:[0,0,0]
	v_mfma_scale_f32_16x16x128_f8f6f4 v[78:81], v[2:9], v[50:57], v[78:81], v227, v226 op_sel_hi:[0,0,0]
	v_mfma_scale_f32_16x16x128_f8f6f4 v[74:77], v[10:17], v[50:57], v[74:77], v227, v226 op_sel_hi:[0,0,0]
	v_mfma_scale_f32_16x16x128_f8f6f4 v[70:73], v[2:9], v[58:65], v[70:73], v227, v226 op_sel_hi:[0,0,0]
	v_mfma_scale_f32_16x16x128_f8f6f4 v[66:69], v[10:17], v[58:65], v[66:69], v227, v226 op_sel_hi:[0,0,0]
	s_setprio 0
	s_barrier
; #define PG8_STAGE(bufoff, gbase, voff) do { _Pragma("unroll") for (int _i = 0; _i < 2; ++_i) \
;         __builtin_amdgcn_global_load_lds((const unsigned*)((const char*)(gbase) + (voff)[_i]), (LAS unsigned*)(lds + (bufoff) + ldsw + _i * 8192), 16, 0, 0); } while (0)
; #define PG8_LDA(dst, b, h) do { _Pragma("unroll") for (int m = 0; m < 4; ++m) _Pragma("unroll") for (int k = 0; k < 2; ++k) dst[m][k] = *(const LAS bf16x8*)(lds + PG8_SA(b, h) + aoff + m * 2048 + k * 1024); } while (0)
; #define PG8_LDB(dst, b, h) do { _Pragma("unroll") for (int n = 0; n < 2; ++n) _Pragma("unroll") for (int k = 0; k < 2; ++k) dst[n][k] = *(const LAS bf16x8*)(lds + PG8_SB(b, h) + boff + n * 2048 + k * 1024); } while (0)
; #define PG8_WAIT_V(n) asm volatile("s_waitcnt vmcnt(" #n ")" ::: "memory")
; #define PG8_WAIT_L(n) asm volatile("s_waitcnt lgkmcnt(" #n ")" ::: "memory")
; #define PG8_BAR __builtin_amdgcn_s_barrier()
; #define PG8_SCHED __builtin_amdgcn_sched_barrier(0)
;     ...
;             PG8_LDB(B0, 1, 0); PG8_LDB(B1, 1, 1); PG8_SCHED; PG8_LDA(At, 1, 0); PG8_STAGE(PG8_SA(0, 1), a2, va[1]);
;             PG8_WAIT_V(8); PG8_WAIT_L(0); PG8_BAR; PG8_MMA(0, 0, At, B0); PG8_MMA(0, 1, At, B1); PG8_BAR; PG8_SCHED;
;             PG8_LDA(At, 1, 1); PG8_STAGE(PG8_SB(1, 0), b3, voffB); PG8_STAGE(PG8_SB(1, 1), b3 + hstep, voffB); PG8_STAGE(PG8_SA(1, 0), a3, va[0]);
;             PG8_WAIT_V(8); PG8_WAIT_L(0); PG8_BAR; PG8_MMA(1, 0, At, B0); PG8_MMA(1, 1, At, B1); PG8_BAR; PG8_SCHED;
;         }
	s_add_i32 s63, 0, 0x18000
	s_add_i32 s64, 0, 0x1c000
	v_add_u32_e32 v14, s63, v219
	v_add_u32_e32 v30, s64, v219
	ds_read_b128 v[2:5], v14
	ds_read_b128 v[6:9], v14 offset:1024
	ds_read_b128 v[10:13], v14 offset:2048
	ds_read_b128 v[14:17], v14 offset:3072
	ds_read_b128 v[18:21], v30
	ds_read_b128 v[22:25], v30 offset:1024
	ds_read_b128 v[26:29], v30 offset:2048
	ds_read_b128 v[30:33], v30 offset:3072
	s_mov_b32 m0, s43
	v_lshl_add_u64 v[214:215], s[38:39], 0, v[214:215]
	ds_read_b128 v[34:37], v225 offset:32768
	ds_read_b128 v[38:41], v225 offset:33792
	ds_read_b128 v[42:45], v225 offset:34816
	ds_read_b128 v[46:49], v225 offset:35840
	ds_read_b128 v[50:53], v225 offset:36864
	ds_read_b128 v[54:57], v225 offset:37888
	ds_read_b128 v[58:61], v225 offset:38912
	ds_read_b128 v[62:65], v225 offset:39936
	global_load_lds_dwordx4 v[214:215], off
	v_lshl_add_u64 v[212:213], s[38:39], 0, v[212:213]
	s_mov_b32 m0, s44
	s_nop 0
	global_load_lds_dwordx4 v[212:213], off
	s_waitcnt vmcnt(8)
	s_waitcnt lgkmcnt(0)
	s_barrier
	s_setprio 1
	s_waitcnt lgkmcnt(0)
	v_mfma_scale_f32_16x16x128_f8f6f4 v[190:193], v[2:9], v[34:41], v[190:193], v227, v226 op_sel_hi:[0,0,0]
	v_mfma_scale_f32_16x16x128_f8f6f4 v[186:189], v[10:17], v[34:41], v[186:189], v227, v226 op_sel_hi:[0,0,0]
	v_mfma_scale_f32_16x16x128_f8f6f4 v[182:185], v[2:9], v[42:49], v[182:185], v227, v226 op_sel_hi:[0,0,0]
	v_mfma_scale_f32_16x16x128_f8f6f4 v[178:181], v[10:17], v[42:49], v[178:181], v227, v226 op_sel_hi:[0,0,0]
	v_mfma_scale_f32_16x16x128_f8f6f4 v[158:161], v[2:9], v[50:57], v[158:161], v227, v226 op_sel_hi:[0,0,0]
	v_mfma_scale_f32_16x16x128_f8f6f4 v[154:157], v[10:17], v[50:57], v[154:157], v227, v226 op_sel_hi:[0,0,0]
	v_mfma_scale_f32_16x16x128_f8f6f4 v[150:153], v[2:9], v[58:65], v[150:153], v227, v226 op_sel_hi:[0,0,0]
	v_mfma_scale_f32_16x16x128_f8f6f4 v[146:149], v[10:17], v[58:65], v[146:149], v227, v226 op_sel_hi:[0,0,0]
	v_mfma_scale_f32_16x16x128_f8f6f4 v[174:177], v[18:25], v[34:41], v[174:177], v227, v226 op_sel_hi:[0,0,0]
	v_mfma_scale_f32_16x16x128_f8f6f4 v[170:173], v[26:33], v[34:41], v[170:173], v227, v226 op_sel_hi:[0,0,0]
	v_mfma_scale_f32_16x16x128_f8f6f4 v[166:169], v[18:25], v[42:49], v[166:169], v227, v226 op_sel_hi:[0,0,0]
	v_mfma_scale_f32_16x16x128_f8f6f4 v[162:165], v[26:33], v[42:49], v[162:165], v227, v226 op_sel_hi:[0,0,0]
	v_mfma_scale_f32_16x16x128_f8f6f4 v[142:145], v[18:25], v[50:57], v[142:145], v227, v226 op_sel_hi:[0,0,0]
	v_mfma_scale_f32_16x16x128_f8f6f4 v[138:141], v[26:33], v[50:57], v[138:141], v227, v226 op_sel_hi:[0,0,0]
	v_mfma_scale_f32_16x16x128_f8f6f4 v[134:137], v[18:25], v[58:65], v[134:137], v227, v226 op_sel_hi:[0,0,0]
	v_mfma_scale_f32_16x16x128_f8f6f4 v[130:133], v[26:33], v[58:65], v[130:133], v227, v226 op_sel_hi:[0,0,0]
	s_setprio 0
	s_barrier
	s_add_i32 s38, s63, s2
	v_lshl_add_u64 v[212:213], v[230:231], 0, s[10:11]
	s_mov_b32 m0, s38
	ds_read_b128 v[34:37], v225 offset:49152
	ds_read_b128 v[38:41], v225 offset:50176
	ds_read_b128 v[42:45], v225 offset:51200
	ds_read_b128 v[46:49], v225 offset:52224
	ds_read_b128 v[50:53], v225 offset:53248
	ds_read_b128 v[54:57], v225 offset:54272
	ds_read_b128 v[58:61], v225 offset:55296
	ds_read_b128 v[62:65], v225 offset:56320
	global_load_lds_dwordx4 v[212:213], off
	s_add_i32 m0, s38, 0x2000
	s_add_u32 s36, s36, 0x40080
	v_lshl_add_u64 v[212:213], v[232:233], 0, s[10:11]
	s_addc_u32 s37, s37, 0
	s_add_i32 s38, s64, s2
	global_load_lds_dwordx4 v[212:213], off
	v_lshl_add_u64 v[212:213], s[36:37], 0, v[198:199]
	s_mov_b32 m0, s38
	s_nop 0
	global_load_lds_dwordx4 v[212:213], off
	v_lshl_add_u64 v[212:213], s[36:37], 0, v[196:197]
	s_add_i32 m0, s38, 0x2000
	s_nop 0
	global_load_lds_dwordx4 v[212:213], off
	v_lshl_add_u64 v[212:213], v[234:235], 0, s[10:11]
	s_mov_b32 m0, s46
	s_nop 0
	global_load_lds_dwordx4 v[212:213], off
	v_lshl_add_u64 v[212:213], v[236:237], 0, s[10:11]
	s_mov_b32 m0, s47
	s_nop 0
	global_load_lds_dwordx4 v[212:213], off
	s_waitcnt vmcnt(8)
	s_waitcnt lgkmcnt(0)
	s_barrier
	s_setprio 1
	s_waitcnt lgkmcnt(0)
	v_mfma_scale_f32_16x16x128_f8f6f4 v[126:129], v[2:9], v[34:41], v[126:129], v227, v226 op_sel_hi:[0,0,0]
	v_mfma_scale_f32_16x16x128_f8f6f4 v[122:125], v[10:17], v[34:41], v[122:125], v227, v226 op_sel_hi:[0,0,0]
	v_mfma_scale_f32_16x16x128_f8f6f4 v[118:121], v[2:9], v[42:49], v[118:121], v227, v226 op_sel_hi:[0,0,0]
	v_mfma_scale_f32_16x16x128_f8f6f4 v[114:117], v[10:17], v[42:49], v[114:117], v227, v226 op_sel_hi:[0,0,0]
	v_mfma_scale_f32_16x16x128_f8f6f4 v[94:97], v[2:9], v[50:57], v[94:97], v227, v226 op_sel_hi:[0,0,0]
	v_mfma_scale_f32_16x16x128_f8f6f4 v[90:93], v[10:17], v[50:57], v[90:93], v227, v226 op_sel_hi:[0,0,0]
	v_mfma_scale_f32_16x16x128_f8f6f4 v[86:89], v[2:9], v[58:65], v[86:89], v227, v226 op_sel_hi:[0,0,0]
	v_mfma_scale_f32_16x16x128_f8f6f4 v[82:85], v[10:17], v[58:65], v[82:85], v227, v226 op_sel_hi:[0,0,0]
	v_mfma_scale_f32_16x16x128_f8f6f4 v[110:113], v[18:25], v[34:41], v[110:113], v227, v226 op_sel_hi:[0,0,0]
	v_mfma_scale_f32_16x16x128_f8f6f4 v[106:109], v[26:33], v[34:41], v[106:109], v227, v226 op_sel_hi:[0,0,0]
	v_mfma_scale_f32_16x16x128_f8f6f4 v[102:105], v[18:25], v[42:49], v[102:105], v227, v226 op_sel_hi:[0,0,0]
	v_mfma_scale_f32_16x16x128_f8f6f4 v[98:101], v[26:33], v[42:49], v[98:101], v227, v226 op_sel_hi:[0,0,0]
	v_mfma_scale_f32_16x16x128_f8f6f4 v[78:81], v[18:25], v[50:57], v[78:81], v227, v226 op_sel_hi:[0,0,0]
	v_mfma_scale_f32_16x16x128_f8f6f4 v[74:77], v[26:33], v[50:57], v[74:77], v227, v226 op_sel_hi:[0,0,0]
	v_mfma_scale_f32_16x16x128_f8f6f4 v[70:73], v[18:25], v[58:65], v[70:73], v227, v226 op_sel_hi:[0,0,0]
	v_mfma_scale_f32_16x16x128_f8f6f4 v[66:69], v[26:33], v[58:65], v[66:69], v227, v226 op_sel_hi:[0,0,0]
	s_setprio 0
	s_barrier
	s_add_i32 s62, s62, 2
	s_add_u32 s27, s27, 0x100
	s_addc_u32 s29, s29, 0
	s_add_u32 s34, s34, 0x100
	s_addc_u32 s35, s35, 0
	s_cmp_gt_u32 s62, 13
	s_cbranch_scc1 .LBB0_1190
